# hand-written P3 projection epilogue (fewer VALU ops) with write-back stores
# speedup vs baseline: 1.0094x; 1.0094x over previous
; __device__ __forceinline__ unsigned cvt_pk_bf16(float lo, float hi) { unsigned r; asm volatile("v_cvt_pk_bf16_f32 %0, %1, %2" : "=v"(r) : "v"(lo), "v"(hi)); return r; }
; __device__ __forceinline__ int fresh_lane() { int l; asm volatile("v_mbcnt_lo_u32_b32 %0, -1, 0\n\tv_mbcnt_hi_u32_b32 %0, -1, %0" : "=v"(l)); return l; }
; __device__ __forceinline__ void store16_wt(__amdgpu_buffer_rsrc_t rsrc, unsigned byte_off, v4u v) { __builtin_amdgcn_raw_buffer_store_b128(v, rsrc, byte_off, 0, 16); }
;     __device__ __forceinline__ void operator()(AccRef acc, const Unit& u, int wr, int wc, int, int) const {
;         const int ln_ = fresh_lane(), fr = ln_ & 15, fq = ln_ >> 4;
;         const int row0 = u.pm * 256 + wr * 64 + fr, col0 = u.pn * 256 + wc * 32 + 8 * fq;
;         const __amdgpu_buffer_rsrc_t rsrc = __builtin_amdgcn_make_buffer_rsrc((void*)O, 0, (int)((size_t)M * DINP * 2), 0x00020000);
;         float rs[8]; rows_rstd(ss, row0, fq, ln_, rs);
; #pragma unroll
;         for (int ai = 0; ai < 2; ++ai)
; #pragma unroll
;             for (int m = 0; m < 4; ++m) {
;                 const int row = row0 + ai * 128 + m * 16;
;                 const float r = rs[ai * 4 + m];
; #pragma unroll
;                 for (int bj = 0; bj < 2; ++bj) {
;                     const f32x4 v0 = acc[ai][bj][m][0] * r, v1 = acc[ai][bj][m][1] * r;
;                     v4u w; w.x = cvt_pk_bf16(v0[0], v0[1]); w.y = cvt_pk_bf16(v0[2], v0[3]); w.z = cvt_pk_bf16(v1[0], v1[1]); w.w = cvt_pk_bf16(v1[2], v1[3]);
;                     store16_wt(rsrc, (unsigned)(((size_t)row * DINP + col0 + bj * 128) * 2), w);
;                 }
.LBB0_342:
	s_lshl_b32 s98, s6, 8
	v_mbcnt_lo_u32_b32 v130, -1, 0
	v_mbcnt_hi_u32_b32 v130, -1, v130
	s_add_i32 s98, s98, s38
	s_lshl_b32 s99, s7, 8
	s_or_b32 s99, s99, s39
	v_and_or_b32 v131, v130, 15, s98
	v_lshrrev_b32_e32 v132, 4, v130
	v_lshl_add_u32 v132, v132, 3, s99
	s_movk_i32 s98, 0x3c00
	v_mul_lo_u32 v131, v131, s98
	v_readlane_b32 s20, v254, 19
	v_readlane_b32 s21, v254, 20
	v_readlane_b32 s22, v254, 21
	v_readlane_b32 s23, v254, 22
	v_add_lshl_u32 v131, v132, v131, 1
	v_mov_b32_e32 v133, v131
	v_mul_f32_e32 v126, v242, v126
	v_mul_f32_e32 v127, v242, v127
	v_mul_f32_e32 v128, v242, v128
	v_mul_f32_e32 v129, v242, v129
	v_mul_f32_e32 v122, v242, v122
	v_mul_f32_e32 v123, v242, v123
	v_mul_f32_e32 v124, v242, v124
	v_mul_f32_e32 v125, v242, v125
	v_cvt_pk_bf16_f32 v148, v126, v127
	v_cvt_pk_bf16_f32 v149, v128, v129
	v_cvt_pk_bf16_f32 v150, v122, v123
	v_cvt_pk_bf16_f32 v151, v124, v125
	buffer_store_dwordx4 v[148:151], v133, s[20:23], 0 offen
	v_mul_f32_e32 v118, v242, v118
	v_mul_f32_e32 v119, v242, v119
	v_mul_f32_e32 v120, v242, v120
	v_mul_f32_e32 v121, v242, v121
	v_mul_f32_e32 v110, v242, v110
	v_mul_f32_e32 v111, v242, v111
	v_mul_f32_e32 v112, v242, v112
	v_mul_f32_e32 v113, v242, v113
	v_cvt_pk_bf16_f32 v152, v118, v119
	v_cvt_pk_bf16_f32 v153, v120, v121
	v_cvt_pk_bf16_f32 v154, v110, v111
	v_cvt_pk_bf16_f32 v155, v112, v113
	buffer_store_dwordx4 v[152:155], v133, s[20:23], 0 offen offset:256
	v_add_u32_e32 v133, 0x78000, v131
	v_mul_f32_e32 v114, v243, v114
	v_mul_f32_e32 v115, v243, v115
	v_mul_f32_e32 v116, v243, v116
	v_mul_f32_e32 v117, v243, v117
	v_mul_f32_e32 v106, v243, v106
	v_mul_f32_e32 v107, v243, v107
	v_mul_f32_e32 v108, v243, v108
	v_mul_f32_e32 v109, v243, v109
	v_cvt_pk_bf16_f32 v156, v114, v115
	v_cvt_pk_bf16_f32 v157, v116, v117
	v_cvt_pk_bf16_f32 v158, v106, v107
	v_cvt_pk_bf16_f32 v159, v108, v109
	buffer_store_dwordx4 v[156:159], v133, s[20:23], 0 offen
	v_mul_f32_e32 v102, v243, v102
	v_mul_f32_e32 v103, v243, v103
	v_mul_f32_e32 v104, v243, v104
	v_mul_f32_e32 v105, v243, v105
	v_mul_f32_e32 v94, v243, v94
	v_mul_f32_e32 v95, v243, v95
	v_mul_f32_e32 v96, v243, v96
	v_mul_f32_e32 v97, v243, v97
	v_cvt_pk_bf16_f32 v160, v102, v103
	v_cvt_pk_bf16_f32 v161, v104, v105
	v_cvt_pk_bf16_f32 v162, v94, v95
	v_cvt_pk_bf16_f32 v163, v96, v97
	buffer_store_dwordx4 v[160:163], v133, s[20:23], 0 offen offset:256
	v_add_u32_e32 v133, 0xf0000, v131
	v_mul_f32_e32 v98, v244, v98
	v_mul_f32_e32 v99, v244, v99
	v_mul_f32_e32 v100, v244, v100
	v_mul_f32_e32 v101, v244, v101
	v_mul_f32_e32 v90, v244, v90
	v_mul_f32_e32 v91, v244, v91
	v_mul_f32_e32 v92, v244, v92
	v_mul_f32_e32 v93, v244, v93
	v_cvt_pk_bf16_f32 v148, v98, v99
	v_cvt_pk_bf16_f32 v149, v100, v101
	v_cvt_pk_bf16_f32 v150, v90, v91
	v_cvt_pk_bf16_f32 v151, v92, v93
	buffer_store_dwordx4 v[148:151], v133, s[20:23], 0 offen
	v_mul_f32_e32 v86, v244, v86
	v_mul_f32_e32 v87, v244, v87
	v_mul_f32_e32 v88, v244, v88
	v_mul_f32_e32 v89, v244, v89
	v_mul_f32_e32 v78, v244, v78
	v_mul_f32_e32 v79, v244, v79
	v_mul_f32_e32 v80, v244, v80
	v_mul_f32_e32 v81, v244, v81
	v_cvt_pk_bf16_f32 v152, v86, v87
	v_cvt_pk_bf16_f32 v153, v88, v89
	v_cvt_pk_bf16_f32 v154, v78, v79
	v_cvt_pk_bf16_f32 v155, v80, v81
	buffer_store_dwordx4 v[152:155], v133, s[20:23], 0 offen offset:256
	v_add_u32_e32 v133, 0x168000, v131
	v_mul_f32_e32 v82, v245, v82
	v_mul_f32_e32 v83, v245, v83
	v_mul_f32_e32 v84, v245, v84
	v_mul_f32_e32 v85, v245, v85
	v_mul_f32_e32 v74, v245, v74
	v_mul_f32_e32 v75, v245, v75
	v_mul_f32_e32 v76, v245, v76
	v_mul_f32_e32 v77, v245, v77
	v_cvt_pk_bf16_f32 v156, v82, v83
	v_cvt_pk_bf16_f32 v157, v84, v85
	v_cvt_pk_bf16_f32 v158, v74, v75
	v_cvt_pk_bf16_f32 v159, v76, v77
	buffer_store_dwordx4 v[156:159], v133, s[20:23], 0 offen
	v_mul_f32_e32 v70, v245, v70
	v_mul_f32_e32 v71, v245, v71
	v_mul_f32_e32 v72, v245, v72
	v_mul_f32_e32 v73, v245, v73
	v_mul_f32_e32 v66, v245, v66
	v_mul_f32_e32 v67, v245, v67
	v_mul_f32_e32 v68, v245, v68
	v_mul_f32_e32 v69, v245, v69
; __device__ __forceinline__ unsigned cvt_pk_bf16(float lo, float hi) { unsigned r; asm volatile("v_cvt_pk_bf16_f32 %0, %1, %2" : "=v"(r) : "v"(lo), "v"(hi)); return r; }
; __device__ __forceinline__ void store16_wt(__amdgpu_buffer_rsrc_t rsrc, unsigned byte_off, v4u v) { __builtin_amdgcn_raw_buffer_store_b128(v, rsrc, byte_off, 0, 16); }
;     __device__ __forceinline__ void operator()(AccRef acc, const Unit& u, int wr, int wc, int, int) const {
;     ...
;         for (int ai = 0; ai < 2; ++ai)
; #pragma unroll
;             for (int m = 0; m < 4; ++m) {
;                 const int row = row0 + ai * 128 + m * 16;
;                 const float r = rs[ai * 4 + m];
; #pragma unroll
;                 for (int bj = 0; bj < 2; ++bj) {
;                     const f32x4 v0 = acc[ai][bj][m][0] * r, v1 = acc[ai][bj][m][1] * r;
;                     v4u w; w.x = cvt_pk_bf16(v0[0], v0[1]); w.y = cvt_pk_bf16(v0[2], v0[3]); w.z = cvt_pk_bf16(v1[0], v1[1]); w.w = cvt_pk_bf16(v1[2], v1[3]);
;                     store16_wt(rsrc, (unsigned)(((size_t)row * DINP + col0 + bj * 128) * 2), w);
;                 }
	v_cvt_pk_bf16_f32 v160, v70, v71
	v_cvt_pk_bf16_f32 v161, v72, v73
	v_cvt_pk_bf16_f32 v162, v66, v67
	v_cvt_pk_bf16_f32 v163, v68, v69
	buffer_store_dwordx4 v[160:163], v133, s[20:23], 0 offen offset:256
	v_add_u32_e32 v133, 0x3c0000, v131
	v_mul_f32_e32 v62, v246, v62
	v_mul_f32_e32 v63, v246, v63
	v_mul_f32_e32 v64, v246, v64
	v_mul_f32_e32 v65, v246, v65
	v_mul_f32_e32 v58, v246, v58
	v_mul_f32_e32 v59, v246, v59
	v_mul_f32_e32 v60, v246, v60
	v_mul_f32_e32 v61, v246, v61
	v_cvt_pk_bf16_f32 v148, v62, v63
	v_cvt_pk_bf16_f32 v149, v64, v65
	v_cvt_pk_bf16_f32 v150, v58, v59
	v_cvt_pk_bf16_f32 v151, v60, v61
	buffer_store_dwordx4 v[148:151], v133, s[20:23], 0 offen
	v_mul_f32_e32 v54, v246, v54
	v_mul_f32_e32 v55, v246, v55
	v_mul_f32_e32 v56, v246, v56
	v_mul_f32_e32 v57, v246, v57
	v_mul_f32_e32 v46, v246, v46
	v_mul_f32_e32 v47, v246, v47
	v_mul_f32_e32 v48, v246, v48
	v_mul_f32_e32 v49, v246, v49
	v_cvt_pk_bf16_f32 v152, v54, v55
	v_cvt_pk_bf16_f32 v153, v56, v57
	v_cvt_pk_bf16_f32 v154, v46, v47
	v_cvt_pk_bf16_f32 v155, v48, v49
	buffer_store_dwordx4 v[152:155], v133, s[20:23], 0 offen offset:256
	v_add_u32_e32 v133, 0x438000, v131
	v_mul_f32_e32 v50, v247, v50
	v_mul_f32_e32 v51, v247, v51
	v_mul_f32_e32 v52, v247, v52
	v_mul_f32_e32 v53, v247, v53
	v_mul_f32_e32 v42, v247, v42
	v_mul_f32_e32 v43, v247, v43
	v_mul_f32_e32 v44, v247, v44
	v_mul_f32_e32 v45, v247, v45
	v_cvt_pk_bf16_f32 v156, v50, v51
	v_cvt_pk_bf16_f32 v157, v52, v53
	v_cvt_pk_bf16_f32 v158, v42, v43
	v_cvt_pk_bf16_f32 v159, v44, v45
	buffer_store_dwordx4 v[156:159], v133, s[20:23], 0 offen
	v_mul_f32_e32 v38, v247, v38
	v_mul_f32_e32 v39, v247, v39
	v_mul_f32_e32 v40, v247, v40
	v_mul_f32_e32 v41, v247, v41
	v_mul_f32_e32 v30, v247, v30
	v_mul_f32_e32 v31, v247, v31
	v_mul_f32_e32 v32, v247, v32
	v_mul_f32_e32 v33, v247, v33
	v_cvt_pk_bf16_f32 v160, v38, v39
	v_cvt_pk_bf16_f32 v161, v40, v41
	v_cvt_pk_bf16_f32 v162, v30, v31
	v_cvt_pk_bf16_f32 v163, v32, v33
	buffer_store_dwordx4 v[160:163], v133, s[20:23], 0 offen offset:256
	v_add_u32_e32 v133, 0x4b0000, v131
	v_mul_f32_e32 v34, v248, v34
	v_mul_f32_e32 v35, v248, v35
	v_mul_f32_e32 v36, v248, v36
	v_mul_f32_e32 v37, v248, v37
	v_mul_f32_e32 v26, v248, v26
	v_mul_f32_e32 v27, v248, v27
	v_mul_f32_e32 v28, v248, v28
	v_mul_f32_e32 v29, v248, v29
	v_cvt_pk_bf16_f32 v148, v34, v35
	v_cvt_pk_bf16_f32 v149, v36, v37
	v_cvt_pk_bf16_f32 v150, v26, v27
	v_cvt_pk_bf16_f32 v151, v28, v29
	buffer_store_dwordx4 v[148:151], v133, s[20:23], 0 offen
	v_mul_f32_e32 v22, v248, v22
	v_mul_f32_e32 v23, v248, v23
	v_mul_f32_e32 v24, v248, v24
	v_mul_f32_e32 v25, v248, v25
	v_mul_f32_e32 v14, v248, v14
	v_mul_f32_e32 v15, v248, v15
	v_mul_f32_e32 v16, v248, v16
	v_mul_f32_e32 v17, v248, v17
	v_cvt_pk_bf16_f32 v152, v22, v23
	v_cvt_pk_bf16_f32 v153, v24, v25
	v_cvt_pk_bf16_f32 v154, v14, v15
	v_cvt_pk_bf16_f32 v155, v16, v17
	buffer_store_dwordx4 v[152:155], v133, s[20:23], 0 offen offset:256
	v_add_u32_e32 v133, 0x528000, v131
	v_mul_f32_e32 v18, v249, v18
	v_mul_f32_e32 v19, v249, v19
	v_mul_f32_e32 v20, v249, v20
	v_mul_f32_e32 v21, v249, v21
	v_mul_f32_e32 v10, v249, v10
	v_mul_f32_e32 v11, v249, v11
	v_mul_f32_e32 v12, v249, v12
	v_mul_f32_e32 v13, v249, v13
	v_cvt_pk_bf16_f32 v156, v18, v19
	v_cvt_pk_bf16_f32 v157, v20, v21
	v_cvt_pk_bf16_f32 v158, v10, v11
	v_cvt_pk_bf16_f32 v159, v12, v13
	buffer_store_dwordx4 v[156:159], v133, s[20:23], 0 offen
	v_mul_f32_e32 v4, v249, v4
	v_mul_f32_e32 v5, v249, v5
	v_mul_f32_e32 v6, v249, v6
	v_mul_f32_e32 v7, v249, v7
	v_mul_f32_e32 v0, v249, v0
	v_mul_f32_e32 v1, v249, v1
	v_mul_f32_e32 v2, v249, v2
	v_mul_f32_e32 v3, v249, v3
	v_cvt_pk_bf16_f32 v160, v4, v5
	v_cvt_pk_bf16_f32 v161, v6, v7
	v_cvt_pk_bf16_f32 v162, v0, v1
	v_cvt_pk_bf16_f32 v163, v2, v3
	buffer_store_dwordx4 v[160:163], v133, s[20:23], 0 offen offset:256
	s_mov_b64 s[6:7], -1
	s_andn2_b64 vcc, exec, s[4:5]
	s_cbranch_vccnz .LBB0_335
	s_andn2_b64 vcc, exec, s[0:1]
	s_cbranch_vccnz .LBB0_334
	s_barrier
	s_branch .LBB0_334
